# static s_setprio 1 on waves 0-3 instead of waves 4-7 (A/B of which half to raise), otherwise v045
# speedup vs baseline: 1.0059x; 1.0059x over previous
_Z6mk_fwd4Args:
	s_load_dword s3, s[0:1], 0xb8
	s_add_u32 s4, s0, 0xb8
	s_addc_u32 s5, s1, 0
	v_readfirstlane_b32 s52, v0
	v_writelane_b32 v252, s4, 0
	s_nop 1
	v_writelane_b32 v252, s5, 1
	s_waitcnt lgkmcnt(0)
	s_cmp_ge_u32 s52, 0x100
	s_cbranch_scc1 .Lprio_skip
	s_setprio 1
